# v34
# baseline (speedup 1.0000x reference)
.LBB0_34:
	s_or_b64 exec, exec, s[10:11]
	ds_read_b128 v[18:21], v72
	s_waitcnt vmcnt(3)
	v_cvt_pk_f16_f32 v14, v14, v15
	v_cvt_pk_f16_f32 v15, v16, v17
	v_cvt_pk_f16_f32 v16, v10, v11
	ds_read_b128 v[22:25], v71 offset:41984
	v_cvt_pk_f16_f32 v17, v12, v13
	ds_read_b128 v[10:13], v72 offset:1024
	ds_read_b128 v[26:29], v71 offset:42048
	s_waitcnt vmcnt(1)
	v_cvt_pk_f16_f32 v0, v6, v7
	v_cvt_pk_f16_f32 v1, v8, v9
	v_cvt_pk_f16_f32 v2, v2, v3
	v_cvt_pk_f16_f32 v3, v4, v5
	s_waitcnt lgkmcnt(2)
	v_mfma_f32_16x16x32_f16 v[30:33], v[18:21], v[14:17], v[22:25]
	s_add_i32 s10, s20, s12
	v_mfma_f32_16x16x32_f16 v[18:21], v[18:21], v[0:3], v[22:25]
	ds_read_b128 v[4:7], v72 offset:2048
	s_nop 1
	ds_read_b128 v[22:25], v71 offset:42112
	s_waitcnt lgkmcnt(2)
	v_mfma_f32_16x16x32_f16 v[34:37], v[10:13], v[14:17], v[26:29]
	v_exp_f32_e32 v78, v30
	v_exp_f32_e32 v79, v31
	v_exp_f32_e32 v20, v20
	v_mfma_f32_16x16x32_f16 v[8:11], v[10:13], v[0:3], v[26:29]
	ds_read_b128 v[44:47], v71 offset:42176
	s_nop 2
	v_exp_f32_e64 v80, v34 clamp
	v_exp_f32_e64 v81, v35 clamp
	ds_read_b128 v[26:29], v72 offset:3072
	s_waitcnt lgkmcnt(2)
	v_mfma_f32_16x16x32_f16 v[48:51], v[4:7], v[14:17], v[22:25]
	v_exp_f32_e64 v82, v36 clamp
	v_exp_f32_e64 v83, v37 clamp
	v_exp_f32_e32 v21, v21
	v_mfma_f32_16x16x32_f16 v[22:25], v[4:7], v[0:3], v[22:25]
	ds_read_b128 v[52:55], v72 offset:4096
	ds_read_b128 v[56:59], v71 offset:42240
	s_nop 1
	v_exp_f32_e32 v4, v48
	s_waitcnt lgkmcnt(2)
	v_mfma_f32_16x16x32_f16 v[60:63], v[26:29], v[14:17], v[44:47]
	v_exp_f32_e32 v5, v49
	v_exp_f32_e32 v48, v32
	v_exp_f32_e32 v49, v33
	v_mfma_f32_16x16x32_f16 v[26:29], v[26:29], v[0:3], v[44:47]
	ds_read_b128 v[64:67], v71 offset:42304
	v_exp_f32_e32 v6, v50
	v_exp_f32_e32 v7, v51
	ds_read_b128 v[44:47], v72 offset:5120
	s_waitcnt lgkmcnt(2)
	v_mfma_f32_16x16x32_f16 v[74:77], v[52:55], v[14:17], v[56:59]
	v_exp_f32_e32 v50, v18
	v_exp_f32_e32 v51, v19
	v_exp_f32_e32 v26, v26
	v_mfma_f32_16x16x32_f16 v[30:33], v[52:55], v[0:3], v[56:59]
	v_exp_f32_e64 v52, v8 clamp
	v_exp_f32_e64 v53, v9 clamp
	v_exp_f32_e32 v8, v22
	s_waitcnt lgkmcnt(0)
	v_mfma_f32_16x16x32_f16 v[34:37], v[44:47], v[14:17], v[64:67]
	v_exp_f32_e32 v9, v23
	v_exp_f32_e64 v22, v10 clamp
	v_exp_f32_e64 v23, v11 clamp
	v_mfma_f32_16x16x32_f16 v[44:47], v[44:47], v[0:3], v[64:67]
	v_exp_f32_e32 v10, v24
	v_exp_f32_e32 v11, v25
	s_nop 1
	v_exp_f32_e32 v12, v34
	v_exp_f32_e32 v13, v35
	v_exp_f32_e32 v18, v36
	v_exp_f32_e32 v24, v60
	v_exp_f32_e32 v25, v61
	v_exp_f32_e64 v54, v74 clamp
	v_exp_f32_e64 v55, v75 clamp
	v_exp_f32_e32 v34, v62
	v_exp_f32_e32 v35, v63
	v_exp_f32_e64 v56, v76 clamp
	v_exp_f32_e64 v57, v77 clamp
	v_exp_f32_e32 v19, v37
	v_exp_f32_e32 v27, v27
	v_exp_f32_e64 v30, v30 clamp
	v_exp_f32_e64 v31, v31 clamp
	v_exp_f32_e32 v36, v44
	v_exp_f32_e32 v37, v45
	v_exp_f32_e32 v28, v28
	v_exp_f32_e32 v29, v29
	v_exp_f32_e64 v32, v32 clamp
	v_exp_f32_e64 v33, v33 clamp
	v_exp_f32_e32 v44, v46
	v_exp_f32_e32 v45, v47
	v_pk_fma_f32 v[58:59], v[80:81], s[2:3], 1.0 op_sel_hi:[1,0,0]
	v_pk_fma_f32 v[60:61], v[82:83], s[2:3], 1.0 op_sel_hi:[1,0,0]
	v_pk_fma_f32 v[52:53], v[52:53], s[2:3], 1.0 op_sel_hi:[1,0,0]
	v_pk_fma_f32 v[22:23], v[22:23], s[2:3], 1.0 op_sel_hi:[1,0,0]
	v_pk_fma_f32 v[54:55], v[54:55], s[2:3], 1.0 op_sel_hi:[1,0,0]
	v_pk_fma_f32 v[56:57], v[56:57], s[2:3], 1.0 op_sel_hi:[1,0,0]
	v_pk_fma_f32 v[30:31], v[30:31], s[2:3], 1.0 op_sel_hi:[1,0,0]
	v_pk_fma_f32 v[32:33], v[32:33], s[2:3], 1.0 op_sel_hi:[1,0,0]
	v_pk_fma_f32 v[46:47], v[78:79], v[58:59], v[58:59]
	v_pk_fma_f32 v[48:49], v[48:49], v[60:61], v[60:61]
	v_pk_fma_f32 v[50:51], v[50:51], v[52:53], v[52:53]
	v_pk_fma_f32 v[20:21], v[20:21], v[22:23], v[22:23]
	v_pk_fma_f32 v[24:25], v[24:25], v[54:55], v[54:55]
	v_pk_fma_f32 v[34:35], v[34:35], v[56:57], v[56:57]
	v_pk_fma_f32 v[26:27], v[26:27], v[30:31], v[30:31]
	v_pk_fma_f32 v[28:29], v[28:29], v[32:33], v[32:33]
	v_pk_fma_f32 v[58:59], v[58:59], s[6:7], v[40:41] op_sel_hi:[1,0,0] neg_lo:[1,0,0] neg_hi:[1,0,0]
	v_pk_fma_f32 v[60:61], v[60:61], s[6:7], v[40:41] op_sel_hi:[1,0,0] neg_lo:[1,0,0] neg_hi:[1,0,0]
	v_pk_fma_f32 v[52:53], v[52:53], s[6:7], v[40:41] op_sel_hi:[1,0,0] neg_lo:[1,0,0] neg_hi:[1,0,0]
	v_pk_fma_f32 v[22:23], v[22:23], s[6:7], v[40:41] op_sel_hi:[1,0,0] neg_lo:[1,0,0] neg_hi:[1,0,0]
	v_pk_fma_f32 v[54:55], v[54:55], s[6:7], v[40:41] op_sel_hi:[1,0,0] neg_lo:[1,0,0] neg_hi:[1,0,0]
	v_pk_fma_f32 v[56:57], v[56:57], s[6:7], v[40:41] op_sel_hi:[1,0,0] neg_lo:[1,0,0] neg_hi:[1,0,0]
	v_pk_fma_f32 v[30:31], v[30:31], s[6:7], v[40:41] op_sel_hi:[1,0,0] neg_lo:[1,0,0] neg_hi:[1,0,0]
	v_pk_fma_f32 v[32:33], v[32:33], s[6:7], v[40:41] op_sel_hi:[1,0,0] neg_lo:[1,0,0] neg_hi:[1,0,0]
	v_pk_fma_f32 v[46:47], v[4:5], v[46:47], v[46:47]
	v_pk_fma_f32 v[48:49], v[6:7], v[48:49], v[48:49]
	v_pk_fma_f32 v[50:51], v[8:9], v[50:51], v[50:51]
	v_pk_fma_f32 v[20:21], v[10:11], v[20:21], v[20:21]
	v_pk_fma_f32 v[24:25], v[12:13], v[24:25], v[24:25]
	v_pk_fma_f32 v[34:35], v[18:19], v[34:35], v[34:35]
	v_pk_fma_f32 v[26:27], v[36:37], v[26:27], v[26:27]
	v_pk_fma_f32 v[28:29], v[44:45], v[28:29], v[28:29]
	v_rcp_f32_e64 v46, v46 clamp
	v_rcp_f32_e64 v47, v47 clamp
	v_rcp_f32_e64 v48, v48 clamp
	v_rcp_f32_e64 v49, v49 clamp
	v_rcp_f32_e64 v50, v50 clamp
	v_rcp_f32_e64 v51, v51 clamp
	v_rcp_f32_e64 v20, v20 clamp
	v_rcp_f32_e64 v21, v21 clamp
	v_rcp_f32_e64 v24, v24 clamp
	v_rcp_f32_e64 v25, v25 clamp
	v_rcp_f32_e64 v34, v34 clamp
	v_rcp_f32_e64 v35, v35 clamp
	v_rcp_f32_e64 v26, v26 clamp
	v_rcp_f32_e64 v27, v27 clamp
	v_rcp_f32_e64 v28, v28 clamp
	v_rcp_f32_e64 v29, v29 clamp
	v_pk_mul_f32 v[46:47], v[58:59], v[46:47]
	v_pk_mul_f32 v[48:49], v[60:61], v[48:49]
	v_pk_mul_f32 v[50:51], v[52:53], v[50:51]
	v_pk_mul_f32 v[20:21], v[22:23], v[20:21]
	v_pk_mul_f32 v[22:23], v[54:55], v[24:25]
	v_pk_mul_f32 v[24:25], v[56:57], v[34:35]
	v_pk_mul_f32 v[26:27], v[30:31], v[26:27]
	v_pk_mul_f32 v[28:29], v[32:33], v[28:29]
	v_pk_fma_f32 v[4:5], v[4:5], v[46:47], v[46:47]
	v_pk_fma_f32 v[6:7], v[6:7], v[48:49], v[48:49]
	v_pk_fma_f32 v[8:9], v[8:9], v[50:51], v[50:51]
	v_pk_fma_f32 v[10:11], v[10:11], v[20:21], v[20:21]
	v_pk_fma_f32 v[12:13], v[12:13], v[22:23], v[22:23]
	v_pk_fma_f32 v[18:19], v[18:19], v[24:25], v[24:25]
	v_pk_fma_f32 v[30:31], v[36:37], v[26:27], v[26:27]
	v_pk_fma_f32 v[32:33], v[44:45], v[28:29], v[28:29]
	s_nop 0
	v_pk_fma_f32 v[4:5], v[4:5], v[4:5], s[4:5] neg_lo:[1,0,0] neg_hi:[1,0,0] clamp
	v_pk_fma_f32 v[6:7], v[6:7], v[6:7], s[4:5] neg_lo:[1,0,0] neg_hi:[1,0,0] clamp
	v_pk_fma_f32 v[8:9], v[8:9], v[8:9], s[4:5] neg_lo:[1,0,0] neg_hi:[1,0,0] clamp
	v_pk_fma_f32 v[10:11], v[10:11], v[10:11], s[4:5] neg_lo:[1,0,0] neg_hi:[1,0,0] clamp
	v_pk_fma_f32 v[12:13], v[12:13], v[12:13], s[4:5] neg_lo:[1,0,0] neg_hi:[1,0,0] clamp
	v_pk_fma_f32 v[18:19], v[18:19], v[18:19], s[4:5] neg_lo:[1,0,0] neg_hi:[1,0,0] clamp
	v_pk_fma_f32 v[30:31], v[30:31], v[30:31], s[4:5] neg_lo:[1,0,0] neg_hi:[1,0,0] clamp
	s_nop 0
	v_pk_fma_f32 v[32:33], v[32:33], v[32:33], s[4:5] neg_lo:[1,0,0] neg_hi:[1,0,0] clamp
	s_nop 0
	v_pk_fma_f32 v[8:9], v[8:9], v[8:9], s[8:9] op_sel_hi:[1,1,0]
	v_pk_fma_f32 v[10:11], v[10:11], v[10:11], s[8:9] op_sel_hi:[1,1,0]
	v_pk_fma_f32 v[12:13], v[12:13], v[12:13], s[8:9] op_sel_hi:[1,1,0]
	v_pk_fma_f32 v[18:19], v[18:19], v[18:19], s[8:9] op_sel_hi:[1,1,0]
	v_pk_fma_f32 v[32:33], v[32:33], v[32:33], s[8:9] op_sel_hi:[1,1,0]
	v_pk_fma_f32 v[4:5], v[4:5], v[4:5], s[8:9] op_sel_hi:[1,1,0]
	v_pk_fma_f32 v[6:7], v[6:7], v[6:7], s[8:9] op_sel_hi:[1,1,0]
	v_pk_fma_f32 v[30:31], v[30:31], v[30:31], s[8:9] op_sel_hi:[1,1,0]
	v_pk_mul_f32 v[8:9], v[50:51], v[8:9]
	v_pk_mul_f32 v[84:85], v[20:21], v[10:11]
	v_pk_mul_f32 v[86:87], v[22:23], v[12:13]
	v_pk_mul_f32 v[10:11], v[24:25], v[18:19]
	v_pk_mul_f32 v[12:13], v[28:29], v[32:33]
	v_pk_mul_f32 v[64:65], v[46:47], v[4:5]
	v_pk_mul_f32 v[82:83], v[48:49], v[6:7]
	v_pk_mul_f32 v[20:21], v[30:31], v[26:27]
	ds_read_b128 v[4:7], v72 offset:6144
	ds_read_b128 v[22:25], v71 offset:42368
	ds_read_b128 v[26:29], v72 offset:7168
	ds_read_b128 v[30:33], v71 offset:42432
	v_cvt_pk_f16_f32 v19, v84, v85
	v_cvt_pk_f16_f32 v18, v8, v9
	v_cvt_pk_f16_f32 v20, v20, v21
	v_cvt_pk_f16_f32 v21, v12, v13
	s_waitcnt lgkmcnt(2)
	v_mfma_f32_16x16x32_f16 v[34:37], v[4:7], v[14:17], v[22:25]
	v_mfma_f32_16x16x32_f16 v[44:47], v[4:7], v[0:3], v[22:25]
	ds_read_b128 v[4:7], v72 offset:8192
	ds_read_b128 v[48:51], v71 offset:42496
	s_waitcnt lgkmcnt(2)
	v_mfma_f32_16x16x32_f16 v[52:55], v[26:29], v[14:17], v[30:33]
	v_cvt_pk_f16_f32 v22, v64, v65
	v_cvt_pk_f16_f32 v23, v82, v83
	v_cvt_pk_f16_f32 v24, v86, v87
	v_mfma_f32_16x16x32_f16 v[26:29], v[26:29], v[0:3], v[30:33]
	ds_read_b128 v[56:59], v71 offset:42560
	v_exp_f32_e32 v86, v34
	v_exp_f32_e32 v87, v35
	ds_read_b128 v[30:33], v72 offset:9216
	s_waitcnt lgkmcnt(2)
	v_mfma_f32_16x16x32_f16 v[60:63], v[4:7], v[14:17], v[48:51]
	v_exp_f32_e64 v88, v52 clamp
	v_exp_f32_e64 v89, v53 clamp
	v_exp_f32_e64 v90, v54 clamp
	v_mfma_f32_16x16x32_f16 v[48:51], v[4:7], v[0:3], v[48:51]
	ds_read_b128 v[64:67], v72 offset:10240
	ds_read_b128 v[74:77], v71 offset:42624
	s_nop 1
	v_exp_f32_e32 v4, v60
	s_waitcnt lgkmcnt(2)
	v_mfma_f32_16x16x32_f16 v[78:81], v[30:33], v[14:17], v[56:59]
	v_exp_f32_e32 v5, v61
	v_exp_f32_e32 v60, v36
	v_exp_f32_e32 v61, v37
	v_mfma_f32_16x16x32_f16 v[30:33], v[30:33], v[0:3], v[56:59]
	ds_read_b128 v[82:85], v71 offset:42688
	v_exp_f32_e64 v91, v55 clamp
	v_exp_f32_e32 v6, v62
	ds_read_b128 v[56:59], v72 offset:11264
	s_waitcnt lgkmcnt(2)
	v_mfma_f32_16x16x32_f16 v[34:37], v[64:67], v[14:17], v[74:77]
	v_exp_f32_e32 v7, v63
	v_exp_f32_e32 v8, v48
	v_exp_f32_e32 v9, v49
	v_mfma_f32_16x16x32_f16 v[52:55], v[64:67], v[0:3], v[74:77]
	v_exp_f32_e32 v44, v44
	v_exp_f32_e32 v45, v45
	v_exp_f32_e64 v26, v26 clamp
	s_waitcnt lgkmcnt(0)
	v_mfma_f32_16x16x32_f16 v[14:17], v[56:59], v[14:17], v[82:85]
	v_exp_f32_e64 v27, v27 clamp
	v_exp_f32_e32 v46, v46
	v_exp_f32_e32 v47, v47
	v_mfma_f32_16x16x32_f16 v[56:59], v[56:59], v[0:3], v[82:85]
	v_exp_f32_e64 v28, v28 clamp
	s_nop 2
	v_exp_f32_e32 v2, v14
	v_exp_f32_e32 v3, v15
	v_exp_f32_e32 v14, v16
	v_exp_f32_e32 v15, v17
	v_exp_f32_e32 v16, v30
	v_exp_f32_e32 v17, v31
	v_exp_f32_e64 v29, v29 clamp
	v_exp_f32_e32 v0, v50
	v_exp_f32_e32 v1, v51
	v_exp_f32_e32 v48, v78
	v_exp_f32_e32 v49, v79
	v_exp_f32_e64 v34, v34 clamp
	v_exp_f32_e64 v35, v35 clamp
	v_exp_f32_e32 v50, v80
	v_exp_f32_e32 v51, v81
	v_exp_f32_e64 v36, v36 clamp
	v_exp_f32_e64 v37, v37 clamp
	v_exp_f32_e64 v30, v52 clamp
	v_exp_f32_e64 v31, v53 clamp
	v_exp_f32_e32 v52, v56
	v_exp_f32_e32 v53, v57
	v_exp_f32_e32 v32, v32
	v_exp_f32_e32 v33, v33
	v_exp_f32_e64 v54, v54 clamp
	v_exp_f32_e64 v55, v55 clamp
	v_exp_f32_e32 v56, v58
	v_cvt_pk_f16_f32 v25, v10, v11
	v_exp_f32_e32 v57, v59
	v_pk_fma_f32 v[30:31], v[30:31], s[2:3], 1.0 op_sel_hi:[1,0,0]
	v_pk_fma_f32 v[10:11], v[88:89], s[2:3], 1.0 op_sel_hi:[1,0,0]
	v_pk_fma_f32 v[12:13], v[90:91], s[2:3], 1.0 op_sel_hi:[1,0,0]
	v_pk_fma_f32 v[26:27], v[26:27], s[2:3], 1.0 op_sel_hi:[1,0,0]
	v_pk_fma_f32 v[28:29], v[28:29], s[2:3], 1.0 op_sel_hi:[1,0,0]
	v_pk_fma_f32 v[34:35], v[34:35], s[2:3], 1.0 op_sel_hi:[1,0,0]
	v_pk_fma_f32 v[36:37], v[36:37], s[2:3], 1.0 op_sel_hi:[1,0,0]
	v_pk_fma_f32 v[54:55], v[54:55], s[2:3], 1.0 op_sel_hi:[1,0,0]
	v_pk_fma_f32 v[16:17], v[16:17], v[30:31], v[30:31]
	v_pk_fma_f32 v[58:59], v[86:87], v[10:11], v[10:11]
	v_pk_fma_f32 v[10:11], v[10:11], s[6:7], v[40:41] op_sel_hi:[1,0,0] neg_lo:[1,0,0] neg_hi:[1,0,0]
	v_pk_fma_f32 v[60:61], v[60:61], v[12:13], v[12:13]
	v_pk_fma_f32 v[12:13], v[12:13], s[6:7], v[40:41] op_sel_hi:[1,0,0] neg_lo:[1,0,0] neg_hi:[1,0,0]
	v_pk_fma_f32 v[44:45], v[44:45], v[26:27], v[26:27]
	v_pk_fma_f32 v[46:47], v[46:47], v[28:29], v[28:29]
	v_pk_fma_f32 v[48:49], v[48:49], v[34:35], v[34:35]
	v_pk_fma_f32 v[50:51], v[50:51], v[36:37], v[36:37]
	v_pk_fma_f32 v[32:33], v[32:33], v[54:55], v[54:55]
	v_pk_fma_f32 v[16:17], v[52:53], v[16:17], v[16:17]
	v_pk_fma_f32 v[26:27], v[26:27], s[6:7], v[40:41] op_sel_hi:[1,0,0] neg_lo:[1,0,0] neg_hi:[1,0,0]
	v_pk_fma_f32 v[28:29], v[28:29], s[6:7], v[40:41] op_sel_hi:[1,0,0] neg_lo:[1,0,0] neg_hi:[1,0,0]
	v_pk_fma_f32 v[34:35], v[34:35], s[6:7], v[40:41] op_sel_hi:[1,0,0] neg_lo:[1,0,0] neg_hi:[1,0,0]
	v_pk_fma_f32 v[36:37], v[36:37], s[6:7], v[40:41] op_sel_hi:[1,0,0] neg_lo:[1,0,0] neg_hi:[1,0,0]
	v_pk_fma_f32 v[30:31], v[30:31], s[6:7], v[40:41] op_sel_hi:[1,0,0] neg_lo:[1,0,0] neg_hi:[1,0,0]
	v_pk_fma_f32 v[54:55], v[54:55], s[6:7], v[40:41] op_sel_hi:[1,0,0] neg_lo:[1,0,0] neg_hi:[1,0,0]
	v_pk_fma_f32 v[58:59], v[4:5], v[58:59], v[58:59]
	v_pk_fma_f32 v[60:61], v[6:7], v[60:61], v[60:61]
	v_pk_fma_f32 v[44:45], v[8:9], v[44:45], v[44:45]
	v_pk_fma_f32 v[46:47], v[0:1], v[46:47], v[46:47]
	v_pk_fma_f32 v[48:49], v[2:3], v[48:49], v[48:49]
	v_pk_fma_f32 v[50:51], v[14:15], v[50:51], v[50:51]
	v_pk_fma_f32 v[32:33], v[56:57], v[32:33], v[32:33]
	v_rcp_f32_e64 v16, v16 clamp
	v_rcp_f32_e64 v17, v17 clamp
	v_rcp_f32_e64 v58, v58 clamp
	v_rcp_f32_e64 v59, v59 clamp
	v_rcp_f32_e64 v60, v60 clamp
	v_rcp_f32_e64 v61, v61 clamp
	v_rcp_f32_e64 v44, v44 clamp
	v_rcp_f32_e64 v45, v45 clamp
	v_rcp_f32_e64 v46, v46 clamp
	v_rcp_f32_e64 v47, v47 clamp
	v_rcp_f32_e64 v48, v48 clamp
	v_rcp_f32_e64 v49, v49 clamp
	v_rcp_f32_e64 v50, v50 clamp
	v_rcp_f32_e64 v51, v51 clamp
	v_rcp_f32_e64 v32, v32 clamp
	v_rcp_f32_e64 v33, v33 clamp
	v_pk_mul_f32 v[10:11], v[10:11], v[58:59]
	v_pk_mul_f32 v[12:13], v[12:13], v[60:61]
	v_pk_mul_f32 v[26:27], v[26:27], v[44:45]
	v_pk_mul_f32 v[34:35], v[34:35], v[48:49]
	v_pk_mul_f32 v[36:37], v[36:37], v[50:51]
	v_pk_mul_f32 v[28:29], v[28:29], v[46:47]
	v_pk_mul_f32 v[16:17], v[30:31], v[16:17]
	v_pk_mul_f32 v[30:31], v[54:55], v[32:33]
	v_pk_fma_f32 v[4:5], v[4:5], v[10:11], v[10:11]
	v_pk_fma_f32 v[6:7], v[6:7], v[12:13], v[12:13]
	v_pk_fma_f32 v[8:9], v[8:9], v[26:27], v[26:27]
	v_pk_fma_f32 v[2:3], v[2:3], v[34:35], v[34:35]
	v_pk_fma_f32 v[14:15], v[14:15], v[36:37], v[36:37]
	v_pk_fma_f32 v[0:1], v[0:1], v[28:29], v[28:29]
	v_pk_fma_f32 v[32:33], v[52:53], v[16:17], v[16:17]
	v_pk_fma_f32 v[44:45], v[56:57], v[30:31], v[30:31]
	s_nop 0
	v_pk_fma_f32 v[4:5], v[4:5], v[4:5], s[4:5] neg_lo:[1,0,0] neg_hi:[1,0,0] clamp
	v_pk_fma_f32 v[6:7], v[6:7], v[6:7], s[4:5] neg_lo:[1,0,0] neg_hi:[1,0,0] clamp
	v_pk_fma_f32 v[8:9], v[8:9], v[8:9], s[4:5] neg_lo:[1,0,0] neg_hi:[1,0,0] clamp
	v_pk_fma_f32 v[0:1], v[0:1], v[0:1], s[4:5] neg_lo:[1,0,0] neg_hi:[1,0,0] clamp
	v_pk_fma_f32 v[2:3], v[2:3], v[2:3], s[4:5] neg_lo:[1,0,0] neg_hi:[1,0,0] clamp
	v_pk_fma_f32 v[14:15], v[14:15], v[14:15], s[4:5] neg_lo:[1,0,0] neg_hi:[1,0,0] clamp
	v_pk_fma_f32 v[32:33], v[32:33], v[32:33], s[4:5] neg_lo:[1,0,0] neg_hi:[1,0,0] clamp
	s_nop 0
	v_pk_fma_f32 v[44:45], v[44:45], v[44:45], s[4:5] neg_lo:[1,0,0] neg_hi:[1,0,0] clamp
	s_nop 0
	v_pk_fma_f32 v[32:33], v[32:33], v[32:33], s[8:9] op_sel_hi:[1,1,0]
	v_pk_fma_f32 v[4:5], v[4:5], v[4:5], s[8:9] op_sel_hi:[1,1,0]
	v_pk_fma_f32 v[6:7], v[6:7], v[6:7], s[8:9] op_sel_hi:[1,1,0]
	v_pk_fma_f32 v[8:9], v[8:9], v[8:9], s[8:9] op_sel_hi:[1,1,0]
	v_pk_fma_f32 v[0:1], v[0:1], v[0:1], s[8:9] op_sel_hi:[1,1,0]
	v_pk_fma_f32 v[2:3], v[2:3], v[2:3], s[8:9] op_sel_hi:[1,1,0]
	v_pk_fma_f32 v[14:15], v[14:15], v[14:15], s[8:9] op_sel_hi:[1,1,0]
	v_pk_fma_f32 v[44:45], v[44:45], v[44:45], s[8:9] op_sel_hi:[1,1,0]
	v_pk_mul_f32 v[16:17], v[32:33], v[16:17]
	v_pk_mul_f32 v[52:53], v[10:11], v[4:5]
	v_pk_mul_f32 v[54:55], v[12:13], v[6:7]
	v_pk_mul_f32 v[26:27], v[26:27], v[8:9]
	v_pk_mul_f32 v[28:29], v[28:29], v[0:1]
	v_pk_mul_f32 v[56:57], v[34:35], v[2:3]
	v_pk_mul_f32 v[58:59], v[36:37], v[14:15]
	v_pk_mul_f32 v[60:61], v[30:31], v[44:45]
	ds_read_b128 v[0:3], v72 offset:12288
	ds_read_b128 v[4:7], v71 offset:42752
	ds_read_b128 v[8:11], v72 offset:13312
	ds_read_b128 v[12:15], v72 offset:14336
	ds_read_b128 v[34:37], v72 offset:15360
	ds_read_b128 v[44:47], v71 offset:42816
	v_cvt_pk_f16_f32 v30, v52, v53
	v_cvt_pk_f16_f32 v26, v26, v27
	v_cvt_pk_f16_f32 v31, v54, v55
	s_waitcnt lgkmcnt(4)
	v_mfma_f32_16x16x32_f16 v[48:51], v[0:3], v[22:25], v[4:7]
	v_cvt_pk_f16_f32 v32, v56, v57
	v_cvt_pk_f16_f32 v33, v58, v59
	v_cvt_pk_f16_f32 v27, v28, v29
	v_mfma_f32_16x16x32_f16 v[0:3], v[0:3], v[18:21], v[4:7]
	v_cvt_pk_f16_f32 v28, v16, v17
	v_cvt_pk_f16_f32 v29, v60, v61
	s_add_i32 s11, s9, s12
	s_waitcnt lgkmcnt(3)
	v_mfma_f32_16x16x32_f16 v[48:51], v[8:11], v[30:33], v[48:51]
	s_cmp_lt_i32 s11, 0x8000
	s_cselect_b32 s10, s11, s10
	s_ashr_i32 s11, s10, 31
	v_mfma_f32_16x16x32_f16 v[52:55], v[8:11], v[26:29], v[0:3]
	ds_read_b128 v[4:7], v72 offset:17408
	ds_read_b128 v[8:11], v71 offset:42880
	s_lshl_b64 s[10:11], s[10:11], 12
	s_add_u32 s10, s10, s36
	s_addc_u32 s11, s11, s37
	ds_read_b128 v[0:3], v72 offset:16384
	s_waitcnt lgkmcnt(3)
	v_mfma_f32_16x16x32_f16 v[56:59], v[12:15], v[22:25], v[44:47]
	v_exp_f32_e32 v106, v48
	v_exp_f32_e32 v107, v49
	v_exp_f32_e32 v110, v50
	v_mfma_f32_16x16x32_f16 v[12:15], v[12:15], v[18:21], v[44:47]
	v_exp_f32_e32 v111, v51
	v_exp_f32_e32 v114, v52
	v_exp_f32_e32 v115, v53
	v_mfma_f32_16x16x32_f16 v[44:47], v[34:37], v[30:33], v[56:59]
	v_mfma_f32_16x16x32_f16 v[56:59], v[34:37], v[26:29], v[12:15]
	ds_read_b128 v[34:37], v72 offset:19456
	ds_read_b128 v[60:63], v71 offset:42944
	s_nop 4
	v_exp_f32_e64 v108, v44 clamp
	ds_read_b128 v[12:15], v72 offset:18432
	s_waitcnt lgkmcnt(3)
	v_mfma_f32_16x16x32_f16 v[64:67], v[0:3], v[22:25], v[8:11]
	v_exp_f32_e64 v109, v45 clamp
	v_exp_f32_e64 v112, v46 clamp
	v_exp_f32_e64 v113, v47 clamp
	v_mfma_f32_16x16x32_f16 v[0:3], v[0:3], v[18:21], v[8:11]
	v_exp_f32_e64 v116, v56 clamp
	v_exp_f32_e64 v117, v57 clamp
	v_exp_f32_e64 v58, v58 clamp
	v_mfma_f32_16x16x32_f16 v[64:67], v[4:7], v[30:33], v[64:67]
	v_exp_f32_e64 v59, v59 clamp
	v_mfma_f32_16x16x32_f16 v[74:77], v[4:7], v[26:29], v[0:3]
	ds_read_b128 v[78:81], v72 offset:20480
	ds_read_b128 v[82:85], v72 offset:21504
	ds_read_b128 v[86:89], v71 offset:43008
	s_waitcnt lgkmcnt(3)
	v_mfma_f32_16x16x32_f16 v[6:9], v[12:15], v[22:25], v[60:63]
	v_mfma_f32_16x16x32_f16 v[60:63], v[12:15], v[18:21], v[60:63]
	global_load_dwordx4 v[10:13], v39, s[10:11] offset:16
	global_load_dwordx4 v[14:17], v39, s[10:11]
	global_load_dwordx4 v[2:5], v39, s[10:11] offset:2064
	v_mfma_f32_16x16x32_f16 v[90:93], v[34:37], v[30:33], v[6:9]
	v_mfma_f32_16x16x32_f16 v[60:63], v[34:37], v[26:29], v[60:63]
	s_nop 1
	global_load_dwordx4 v[6:9], v39, s[10:11] offset:2048
	ds_read_b128 v[94:97], v72 offset:22528
	ds_read_b128 v[98:101], v72 offset:23552
	ds_read_b128 v[102:105], v71 offset:43072
	s_waitcnt lgkmcnt(3)
	v_mfma_f32_16x16x32_f16 v[44:47], v[78:81], v[22:25], v[86:89]
	v_exp_f32_e32 v0, v64
	v_exp_f32_e32 v1, v65
	v_exp_f32_e32 v34, v66
	v_mfma_f32_16x16x32_f16 v[48:51], v[78:81], v[18:21], v[86:89]
	v_exp_f32_e32 v35, v67
	v_exp_f32_e32 v36, v74
	v_exp_f32_e32 v37, v75
	v_mfma_f32_16x16x32_f16 v[64:67], v[82:85], v[30:33], v[44:47]
	v_exp_f32_e32 v74, v54
	v_exp_f32_e32 v75, v55
	v_exp_f32_e32 v78, v92
	v_mfma_f32_16x16x32_f16 v[50:53], v[82:85], v[26:29], v[48:51]
	v_exp_f32_e32 v44, v76
	v_exp_f32_e32 v45, v77
	v_exp_f32_e32 v76, v90
	s_waitcnt lgkmcnt(0)
	v_mfma_f32_16x16x32_f16 v[46:49], v[94:97], v[22:25], v[102:105]
	v_exp_f32_e32 v77, v91
	v_exp_f32_e64 v64, v64 clamp
	v_exp_f32_e64 v65, v65 clamp
	v_mfma_f32_16x16x32_f16 v[54:57], v[94:97], v[18:21], v[102:105]
	v_exp_f32_e32 v79, v93
	v_exp_f32_e64 v66, v66 clamp
	v_exp_f32_e64 v67, v67 clamp
	v_mfma_f32_16x16x32_f16 v[46:49], v[98:101], v[30:33], v[46:49]
	v_exp_f32_e32 v60, v60
	v_exp_f32_e32 v61, v61
	v_exp_f32_e64 v50, v50 clamp
	v_mfma_f32_16x16x32_f16 v[54:57], v[98:101], v[26:29], v[54:57]
	v_exp_f32_e64 v51, v51 clamp
	s_nop 2
	v_exp_f32_e32 v46, v46
	v_exp_f32_e32 v47, v47
	v_exp_f32_e32 v48, v48
	v_exp_f32_e32 v49, v49
	v_exp_f32_e32 v54, v54
	v_exp_f32_e32 v55, v55
	v_exp_f32_e32 v62, v62
	v_exp_f32_e32 v63, v63
	v_exp_f32_e64 v52, v52 clamp
	v_exp_f32_e64 v53, v53 clamp
	v_exp_f32_e32 v56, v56
	v_exp_f32_e32 v57, v57
	v_pk_fma_f32 v[80:81], v[108:109], s[2:3], 1.0 op_sel_hi:[1,0,0]
	v_pk_fma_f32 v[82:83], v[112:113], s[2:3], 1.0 op_sel_hi:[1,0,0]
	v_pk_fma_f32 v[84:85], v[116:117], s[2:3], 1.0 op_sel_hi:[1,0,0]
	v_pk_fma_f32 v[58:59], v[58:59], s[2:3], 1.0 op_sel_hi:[1,0,0]
	v_pk_fma_f32 v[64:65], v[64:65], s[2:3], 1.0 op_sel_hi:[1,0,0]
	v_pk_fma_f32 v[66:67], v[66:67], s[2:3], 1.0 op_sel_hi:[1,0,0]
	v_pk_fma_f32 v[50:51], v[50:51], s[2:3], 1.0 op_sel_hi:[1,0,0]
	v_pk_fma_f32 v[52:53], v[52:53], s[2:3], 1.0 op_sel_hi:[1,0,0]
	v_pk_fma_f32 v[86:87], v[106:107], v[80:81], v[80:81]
	v_pk_fma_f32 v[88:89], v[110:111], v[82:83], v[82:83]
	v_pk_fma_f32 v[90:91], v[114:115], v[84:85], v[84:85]
	v_pk_fma_f32 v[74:75], v[74:75], v[58:59], v[58:59]
	v_pk_fma_f32 v[76:77], v[76:77], v[64:65], v[64:65]
	v_pk_fma_f32 v[78:79], v[78:79], v[66:67], v[66:67]
	v_pk_fma_f32 v[60:61], v[60:61], v[50:51], v[50:51]
	v_pk_fma_f32 v[62:63], v[62:63], v[52:53], v[52:53]
	v_pk_fma_f32 v[80:81], v[80:81], s[6:7], v[40:41] op_sel_hi:[1,0,0] neg_lo:[1,0,0] neg_hi:[1,0,0]
	v_pk_fma_f32 v[82:83], v[82:83], s[6:7], v[40:41] op_sel_hi:[1,0,0] neg_lo:[1,0,0] neg_hi:[1,0,0]
	v_pk_fma_f32 v[84:85], v[84:85], s[6:7], v[40:41] op_sel_hi:[1,0,0] neg_lo:[1,0,0] neg_hi:[1,0,0]
	v_pk_fma_f32 v[58:59], v[58:59], s[6:7], v[40:41] op_sel_hi:[1,0,0] neg_lo:[1,0,0] neg_hi:[1,0,0]
	v_pk_fma_f32 v[64:65], v[64:65], s[6:7], v[40:41] op_sel_hi:[1,0,0] neg_lo:[1,0,0] neg_hi:[1,0,0]
	v_pk_fma_f32 v[66:67], v[66:67], s[6:7], v[40:41] op_sel_hi:[1,0,0] neg_lo:[1,0,0] neg_hi:[1,0,0]
	v_pk_fma_f32 v[50:51], v[50:51], s[6:7], v[40:41] op_sel_hi:[1,0,0] neg_lo:[1,0,0] neg_hi:[1,0,0]
	v_pk_fma_f32 v[52:53], v[52:53], s[6:7], v[40:41] op_sel_hi:[1,0,0] neg_lo:[1,0,0] neg_hi:[1,0,0]
	v_pk_fma_f32 v[86:87], v[0:1], v[86:87], v[86:87]
	v_pk_fma_f32 v[88:89], v[34:35], v[88:89], v[88:89]
	v_pk_fma_f32 v[90:91], v[36:37], v[90:91], v[90:91]
	v_pk_fma_f32 v[74:75], v[44:45], v[74:75], v[74:75]
	v_pk_fma_f32 v[76:77], v[46:47], v[76:77], v[76:77]
	v_pk_fma_f32 v[78:79], v[48:49], v[78:79], v[78:79]
	v_pk_fma_f32 v[60:61], v[54:55], v[60:61], v[60:61]
	v_pk_fma_f32 v[62:63], v[56:57], v[62:63], v[62:63]
	v_rcp_f32_e64 v86, v86 clamp
	v_rcp_f32_e64 v87, v87 clamp
	v_rcp_f32_e64 v88, v88 clamp
	v_rcp_f32_e64 v89, v89 clamp
	v_rcp_f32_e64 v90, v90 clamp
	v_rcp_f32_e64 v91, v91 clamp
	v_rcp_f32_e64 v74, v74 clamp
	v_rcp_f32_e64 v75, v75 clamp
	v_rcp_f32_e64 v76, v76 clamp
	v_rcp_f32_e64 v77, v77 clamp
	v_rcp_f32_e64 v78, v78 clamp
	v_rcp_f32_e64 v79, v79 clamp
	v_rcp_f32_e64 v60, v60 clamp
	v_rcp_f32_e64 v61, v61 clamp
	v_rcp_f32_e64 v62, v62 clamp
	v_rcp_f32_e64 v63, v63 clamp
	v_pk_mul_f32 v[80:81], v[80:81], v[86:87]
	v_pk_mul_f32 v[82:83], v[82:83], v[88:89]
	v_pk_mul_f32 v[84:85], v[84:85], v[90:91]
	v_pk_mul_f32 v[58:59], v[58:59], v[74:75]
	v_pk_mul_f32 v[64:65], v[64:65], v[76:77]
	v_pk_mul_f32 v[66:67], v[66:67], v[78:79]
	v_pk_mul_f32 v[50:51], v[50:51], v[60:61]
	v_pk_mul_f32 v[60:61], v[52:53], v[62:63]
	v_pk_fma_f32 v[0:1], v[0:1], v[80:81], v[80:81]
	v_pk_fma_f32 v[34:35], v[34:35], v[82:83], v[82:83]
	v_pk_fma_f32 v[36:37], v[36:37], v[84:85], v[84:85]
	v_pk_fma_f32 v[44:45], v[44:45], v[58:59], v[58:59]
	v_pk_fma_f32 v[46:47], v[46:47], v[64:65], v[64:65]
	v_pk_fma_f32 v[48:49], v[48:49], v[66:67], v[66:67]
	v_pk_fma_f32 v[52:53], v[54:55], v[50:51], v[50:51]
	v_pk_fma_f32 v[54:55], v[56:57], v[60:61], v[60:61]
	s_nop 0
	v_pk_fma_f32 v[0:1], v[0:1], v[0:1], s[4:5] neg_lo:[1,0,0] neg_hi:[1,0,0] clamp
	v_pk_fma_f32 v[34:35], v[34:35], v[34:35], s[4:5] neg_lo:[1,0,0] neg_hi:[1,0,0] clamp
	v_pk_fma_f32 v[36:37], v[36:37], v[36:37], s[4:5] neg_lo:[1,0,0] neg_hi:[1,0,0] clamp
	v_pk_fma_f32 v[44:45], v[44:45], v[44:45], s[4:5] neg_lo:[1,0,0] neg_hi:[1,0,0] clamp
	v_pk_fma_f32 v[46:47], v[46:47], v[46:47], s[4:5] neg_lo:[1,0,0] neg_hi:[1,0,0] clamp
	v_pk_fma_f32 v[48:49], v[48:49], v[48:49], s[4:5] neg_lo:[1,0,0] neg_hi:[1,0,0] clamp
	v_pk_fma_f32 v[52:53], v[52:53], v[52:53], s[4:5] neg_lo:[1,0,0] neg_hi:[1,0,0] clamp
	s_nop 0
	v_pk_fma_f32 v[54:55], v[54:55], v[54:55], s[4:5] neg_lo:[1,0,0] neg_hi:[1,0,0] clamp
	s_nop 0
	v_pk_fma_f32 v[0:1], v[0:1], v[0:1], s[8:9] op_sel_hi:[1,1,0]
	v_pk_fma_f32 v[56:57], v[34:35], v[34:35], s[8:9] op_sel_hi:[1,1,0]
	v_pk_fma_f32 v[36:37], v[36:37], v[36:37], s[8:9] op_sel_hi:[1,1,0]
	v_pk_fma_f32 v[44:45], v[44:45], v[44:45], s[8:9] op_sel_hi:[1,1,0]
	v_pk_fma_f32 v[46:47], v[46:47], v[46:47], s[8:9] op_sel_hi:[1,1,0]
	v_pk_fma_f32 v[48:49], v[48:49], v[48:49], s[8:9] op_sel_hi:[1,1,0]
	v_pk_fma_f32 v[62:63], v[52:53], v[52:53], s[8:9] op_sel_hi:[1,1,0]
	v_pk_fma_f32 v[74:75], v[54:55], v[54:55], s[8:9] op_sel_hi:[1,1,0]
	v_pk_mul_f32 v[34:35], v[80:81], v[0:1]
	v_pk_mul_f32 v[56:57], v[82:83], v[56:57]
	v_pk_mul_f32 v[36:37], v[84:85], v[36:37]
	v_pk_mul_f32 v[52:53], v[58:59], v[44:45]
	v_pk_mul_f32 v[54:55], v[64:65], v[46:47]
	v_pk_mul_f32 v[0:1], v[66:67], v[48:49]
	v_pk_mul_f32 v[46:47], v[62:63], v[50:51]
	v_pk_mul_f32 v[44:45], v[60:61], v[74:75]
	s_cmp_lt_u32 s33, 8
	s_cbranch_scc1 .Lprio_q
	s_setprio 0
.Lprio_q:
	ds_read_b128 v[48:51], v72 offset:24576
	ds_read_b128 v[58:61], v71 offset:43136
	ds_read_b128 v[62:65], v72 offset:25600
	ds_read_b128 v[74:77], v72 offset:26624
	ds_read_b128 v[78:81], v72 offset:27648
	ds_read_b128 v[82:85], v71 offset:43200
	v_cvt_pk_f16_f32 v34, v34, v35
	v_cvt_pk_f16_f32 v35, v56, v57
	s_waitcnt lgkmcnt(4)
	v_mfma_f32_16x16x32_f16 v[86:89], v[48:51], v[22:25], v[58:61]
	v_mfma_f32_16x16x32_f16 v[48:51], v[48:51], v[18:21], v[58:61]
	s_waitcnt lgkmcnt(3)
	v_mfma_f32_16x16x32_f16 v[58:61], v[62:65], v[30:33], v[86:89]
	v_mfma_f32_16x16x32_f16 v[86:89], v[62:65], v[26:29], v[48:51]
	ds_read_b128 v[62:65], v72 offset:29696
	ds_read_b128 v[90:93], v71 offset:43264
	s_nop 2
	ds_read_b128 v[48:51], v72 offset:28672
	s_waitcnt lgkmcnt(3)
	v_mfma_f32_16x16x32_f16 v[94:97], v[74:77], v[22:25], v[82:85]
	v_exp_f32_e32 v120, v86
	v_exp_f32_e32 v121, v87
	v_exp_f32_e32 v122, v88
	v_mfma_f32_16x16x32_f16 v[74:77], v[74:77], v[18:21], v[82:85]
	v_exp_f32_e32 v123, v89
	v_mfma_f32_16x16x32_f16 v[82:85], v[78:81], v[30:33], v[94:97]
	v_mfma_f32_16x16x32_f16 v[74:77], v[78:81], v[26:29], v[74:77]
	ds_read_b128 v[78:81], v72 offset:30720
	s_nop 0
	ds_read_b128 v[94:97], v72 offset:31744
	ds_read_b128 v[98:101], v71 offset:43328
	s_waitcnt lgkmcnt(3)
	v_mfma_f32_16x16x32_f16 v[102:105], v[48:51], v[22:25], v[90:93]
	s_nop 0
	v_exp_f32_e64 v66, v82 clamp
	v_exp_f32_e64 v67, v83 clamp
	v_exp_f32_e64 v118, v84 clamp
	v_mfma_f32_16x16x32_f16 v[48:51], v[48:51], v[18:21], v[90:93]
	v_exp_f32_e64 v119, v85 clamp
	v_exp_f32_e64 v124, v74 clamp
	v_exp_f32_e64 v125, v75 clamp
	v_mfma_f32_16x16x32_f16 v[90:93], v[62:65], v[30:33], v[102:105]
	v_exp_f32_e64 v126, v76 clamp
	v_exp_f32_e64 v127, v77 clamp
	v_mfma_f32_16x16x32_f16 v[102:105], v[62:65], v[26:29], v[48:51]
	ds_read_b128 v[106:109], v72 offset:32768
	ds_read_b128 v[110:113], v72 offset:33792
	v_exp_f32_e32 v62, v58
	v_exp_f32_e32 v63, v59
	v_exp_f32_e32 v64, v60
	v_exp_f32_e32 v65, v61
	ds_read_b128 v[114:117], v71 offset:43392
	s_waitcnt lgkmcnt(3)
	v_mfma_f32_16x16x32_f16 v[58:61], v[78:81], v[22:25], v[98:101]
	v_exp_f32_e32 v48, v90
	v_exp_f32_e32 v49, v91
	v_exp_f32_e32 v50, v92
	v_mfma_f32_16x16x32_f16 v[78:81], v[78:81], v[18:21], v[98:101]
	v_exp_f32_e32 v51, v93
	v_mfma_f32_16x16x32_f16 v[82:85], v[94:97], v[30:33], v[58:61]
	v_mfma_f32_16x16x32_f16 v[78:81], v[94:97], v[26:29], v[78:81]
	ds_read_b128 v[86:89], v72 offset:34816
	ds_read_b128 v[90:93], v72 offset:35840
	ds_read_b128 v[94:97], v71 offset:43456
	s_waitcnt lgkmcnt(3)
	v_mfma_f32_16x16x32_f16 v[74:77], v[106:109], v[22:25], v[114:117]
	v_exp_f32_e32 v58, v102
	v_exp_f32_e32 v59, v103
	v_exp_f32_e32 v60, v104
	v_mfma_f32_16x16x32_f16 v[98:101], v[106:109], v[18:21], v[114:117]
	v_exp_f32_e32 v61, v105
	v_exp_f32_e32 v102, v82
	v_exp_f32_e32 v103, v83
	v_exp_f32_e32 v104, v84
	v_exp_f32_e32 v105, v85
	v_mfma_f32_16x16x32_f16 v[74:77], v[110:113], v[30:33], v[74:77]
	v_mfma_f32_16x16x32_f16 v[82:85], v[110:113], v[26:29], v[98:101]
	s_waitcnt lgkmcnt(0)
	v_mfma_f32_16x16x32_f16 v[18:21], v[86:89], v[18:21], v[94:97]
	s_nop 4
	v_exp_f32_e64 v106, v74 clamp
	v_exp_f32_e64 v107, v75 clamp
	v_exp_f32_e64 v108, v76 clamp
	v_exp_f32_e64 v109, v77 clamp
	v_mfma_f32_16x16x32_f16 v[74:77], v[86:89], v[22:25], v[94:97]
	v_cvt_pk_f16_f32 v22, v36, v37
	v_cvt_pk_f16_f32 v23, v52, v53
	v_cvt_pk_f16_f32 v36, v54, v55
	v_mfma_f32_16x16x32_f16 v[18:21], v[90:93], v[26:29], v[18:21]
	v_exp_f32_e32 v52, v78
	v_exp_f32_e32 v53, v79
	v_exp_f32_e64 v54, v82 clamp
	v_mfma_f32_16x16x32_f16 v[30:33], v[90:93], v[30:33], v[74:77]
	v_exp_f32_e64 v55, v83 clamp
	s_nop 2
	v_exp_f32_e32 v18, v18
	v_exp_f32_e32 v19, v19
	v_exp_f32_e32 v26, v80
	v_exp_f32_e32 v27, v81
	v_exp_f32_e32 v30, v30
	v_exp_f32_e32 v31, v31
	v_exp_f32_e32 v32, v32
	v_exp_f32_e32 v33, v33
	v_exp_f32_e64 v28, v84 clamp
	v_exp_f32_e64 v29, v85 clamp
	v_exp_f32_e32 v20, v20
	v_cvt_pk_f16_f32 v24, v46, v47
	v_cvt_pk_f16_f32 v37, v0, v1
	v_cvt_pk_f16_f32 v25, v44, v45
	v_exp_f32_e32 v21, v21
	v_pk_fma_f32 v[0:1], v[66:67], s[2:3], 1.0 op_sel_hi:[1,0,0]
	v_pk_fma_f32 v[44:45], v[118:119], s[2:3], 1.0 op_sel_hi:[1,0,0]
	v_pk_fma_f32 v[46:47], v[124:125], s[2:3], 1.0 op_sel_hi:[1,0,0]
	v_pk_fma_f32 v[56:57], v[126:127], s[2:3], 1.0 op_sel_hi:[1,0,0]
	v_pk_fma_f32 v[66:67], v[106:107], s[2:3], 1.0 op_sel_hi:[1,0,0]
	v_pk_fma_f32 v[74:75], v[108:109], s[2:3], 1.0 op_sel_hi:[1,0,0]
	v_pk_fma_f32 v[54:55], v[54:55], s[2:3], 1.0 op_sel_hi:[1,0,0]
	v_pk_fma_f32 v[28:29], v[28:29], s[2:3], 1.0 op_sel_hi:[1,0,0]
	v_pk_fma_f32 v[62:63], v[62:63], v[0:1], v[0:1]
	v_pk_fma_f32 v[64:65], v[64:65], v[44:45], v[44:45]
	v_pk_fma_f32 v[76:77], v[120:121], v[46:47], v[46:47]
	v_pk_fma_f32 v[78:79], v[122:123], v[56:57], v[56:57]
	v_pk_fma_f32 v[80:81], v[102:103], v[66:67], v[66:67]
	v_pk_fma_f32 v[82:83], v[104:105], v[74:75], v[74:75]
	v_pk_fma_f32 v[52:53], v[52:53], v[54:55], v[54:55]
	v_pk_fma_f32 v[26:27], v[26:27], v[28:29], v[28:29]
	v_pk_fma_f32 v[0:1], v[0:1], s[6:7], v[40:41] op_sel_hi:[1,0,0] neg_lo:[1,0,0] neg_hi:[1,0,0]
	v_pk_fma_f32 v[44:45], v[44:45], s[6:7], v[40:41] op_sel_hi:[1,0,0] neg_lo:[1,0,0] neg_hi:[1,0,0]
	v_pk_fma_f32 v[46:47], v[46:47], s[6:7], v[40:41] op_sel_hi:[1,0,0] neg_lo:[1,0,0] neg_hi:[1,0,0]
	v_pk_fma_f32 v[56:57], v[56:57], s[6:7], v[40:41] op_sel_hi:[1,0,0] neg_lo:[1,0,0] neg_hi:[1,0,0]
	v_pk_fma_f32 v[66:67], v[66:67], s[6:7], v[40:41] op_sel_hi:[1,0,0] neg_lo:[1,0,0] neg_hi:[1,0,0]
	v_pk_fma_f32 v[74:75], v[74:75], s[6:7], v[40:41] op_sel_hi:[1,0,0] neg_lo:[1,0,0] neg_hi:[1,0,0]
	v_pk_fma_f32 v[54:55], v[54:55], s[6:7], v[40:41] op_sel_hi:[1,0,0] neg_lo:[1,0,0] neg_hi:[1,0,0]
	v_pk_fma_f32 v[28:29], v[28:29], s[6:7], v[40:41] op_sel_hi:[1,0,0] neg_lo:[1,0,0] neg_hi:[1,0,0]
	v_pk_fma_f32 v[62:63], v[48:49], v[62:63], v[62:63]
	v_pk_fma_f32 v[64:65], v[50:51], v[64:65], v[64:65]
	v_pk_fma_f32 v[76:77], v[58:59], v[76:77], v[76:77]
	v_pk_fma_f32 v[78:79], v[60:61], v[78:79], v[78:79]
	v_pk_fma_f32 v[80:81], v[30:31], v[80:81], v[80:81]
	v_pk_fma_f32 v[82:83], v[32:33], v[82:83], v[82:83]
	v_pk_fma_f32 v[52:53], v[18:19], v[52:53], v[52:53]
	v_pk_fma_f32 v[26:27], v[20:21], v[26:27], v[26:27]
	v_rcp_f32_e64 v62, v62 clamp
	v_rcp_f32_e64 v63, v63 clamp
	v_rcp_f32_e64 v64, v64 clamp
	v_rcp_f32_e64 v65, v65 clamp
	v_rcp_f32_e64 v76, v76 clamp
	v_rcp_f32_e64 v77, v77 clamp
	v_rcp_f32_e64 v78, v78 clamp
	v_rcp_f32_e64 v79, v79 clamp
	v_rcp_f32_e64 v80, v80 clamp
	v_rcp_f32_e64 v81, v81 clamp
	v_rcp_f32_e64 v82, v82 clamp
	v_rcp_f32_e64 v83, v83 clamp
	v_rcp_f32_e64 v52, v52 clamp
	v_rcp_f32_e64 v53, v53 clamp
	v_rcp_f32_e64 v26, v26 clamp
	v_rcp_f32_e64 v27, v27 clamp
	v_pk_mul_f32 v[52:53], v[54:55], v[52:53]
	v_pk_mul_f32 v[0:1], v[0:1], v[62:63]
	v_pk_mul_f32 v[44:45], v[44:45], v[64:65]
	v_pk_mul_f32 v[46:47], v[46:47], v[76:77]
	v_pk_mul_f32 v[56:57], v[56:57], v[78:79]
	v_pk_mul_f32 v[62:63], v[66:67], v[80:81]
	v_pk_mul_f32 v[64:65], v[74:75], v[82:83]
	v_pk_mul_f32 v[26:27], v[28:29], v[26:27]
	v_pk_fma_f32 v[18:19], v[18:19], v[52:53], v[52:53]
	v_pk_fma_f32 v[28:29], v[48:49], v[0:1], v[0:1]
	v_pk_fma_f32 v[48:49], v[50:51], v[44:45], v[44:45]
	v_pk_fma_f32 v[50:51], v[58:59], v[46:47], v[46:47]
	v_pk_fma_f32 v[54:55], v[60:61], v[56:57], v[56:57]
	v_pk_fma_f32 v[30:31], v[30:31], v[62:63], v[62:63]
	v_pk_fma_f32 v[32:33], v[32:33], v[64:65], v[64:65]
	v_pk_fma_f32 v[20:21], v[20:21], v[26:27], v[26:27]
	s_nop 0
	v_pk_fma_f32 v[28:29], v[28:29], v[28:29], s[4:5] neg_lo:[1,0,0] neg_hi:[1,0,0] clamp
	v_pk_fma_f32 v[48:49], v[48:49], v[48:49], s[4:5] neg_lo:[1,0,0] neg_hi:[1,0,0] clamp
	v_pk_fma_f32 v[50:51], v[50:51], v[50:51], s[4:5] neg_lo:[1,0,0] neg_hi:[1,0,0] clamp
	v_pk_fma_f32 v[54:55], v[54:55], v[54:55], s[4:5] neg_lo:[1,0,0] neg_hi:[1,0,0] clamp
	v_pk_fma_f32 v[30:31], v[30:31], v[30:31], s[4:5] neg_lo:[1,0,0] neg_hi:[1,0,0] clamp
	v_pk_fma_f32 v[32:33], v[32:33], v[32:33], s[4:5] neg_lo:[1,0,0] neg_hi:[1,0,0] clamp
	v_pk_fma_f32 v[18:19], v[18:19], v[18:19], s[4:5] neg_lo:[1,0,0] neg_hi:[1,0,0] clamp
	s_nop 0
	v_pk_fma_f32 v[20:21], v[20:21], v[20:21], s[4:5] neg_lo:[1,0,0] neg_hi:[1,0,0] clamp
	s_nop 0
	v_pk_fma_f32 v[28:29], v[28:29], v[28:29], s[8:9] op_sel_hi:[1,1,0]
	v_pk_fma_f32 v[48:49], v[48:49], v[48:49], s[8:9] op_sel_hi:[1,1,0]
	v_pk_fma_f32 v[50:51], v[50:51], v[50:51], s[8:9] op_sel_hi:[1,1,0]
	v_pk_fma_f32 v[54:55], v[54:55], v[54:55], s[8:9] op_sel_hi:[1,1,0]
	v_pk_fma_f32 v[30:31], v[30:31], v[30:31], s[8:9] op_sel_hi:[1,1,0]
	v_pk_fma_f32 v[32:33], v[32:33], v[32:33], s[8:9] op_sel_hi:[1,1,0]
	v_pk_fma_f32 v[18:19], v[18:19], v[18:19], s[8:9] op_sel_hi:[1,1,0]
	v_pk_fma_f32 v[20:21], v[20:21], v[20:21], s[8:9] op_sel_hi:[1,1,0]
	v_pk_mul_f32 v[0:1], v[0:1], v[28:29]
	v_pk_mul_f32 v[58:59], v[44:45], v[48:49]
	v_pk_mul_f32 v[60:61], v[46:47], v[50:51]
	v_pk_mul_f32 v[54:55], v[56:57], v[54:55]
	v_pk_mul_f32 v[62:63], v[62:63], v[30:31]
	v_pk_mul_f32 v[64:65], v[64:65], v[32:33]
	v_pk_mul_f32 v[66:67], v[18:19], v[52:53]
	v_pk_mul_f32 v[74:75], v[26:27], v[20:21]
	ds_read_b128 v[18:21], v72 offset:36864
	ds_read_b128 v[30:33], v72 offset:37888
	ds_read_b128 v[26:29], v71 offset:43520
	v_cvt_pk_f16_f32 v56, v60, v61
	v_cvt_pk_f16_f32 v57, v54, v55
	v_cvt_pk_f16_f32 v54, v62, v63
	ds_read_b128 v[60:63], v71 offset:43584
	v_cvt_pk_f16_f32 v52, v0, v1
	v_cvt_pk_f16_f32 v53, v58, v59
	s_waitcnt lgkmcnt(1)
	v_mfma_f32_16x16x32_f16 v[48:51], v[18:21], v[34:37], v[26:29]
	v_cvt_pk_f16_f32 v55, v64, v65
	v_cvt_pk_f16_f32 v58, v66, v67
	v_cvt_pk_f16_f32 v59, v74, v75
	v_mfma_f32_16x16x32_f16 v[18:21], v[18:21], v[22:25], v[26:29]
	ds_read_b128 v[44:47], v72 offset:40960
	s_add_i32 s12, s12, s3
	s_add_i32 s10, s20, s12
	v_mfma_f32_16x16x32_f16 v[26:29], v[30:33], v[52:55], v[48:51]
	s_cmp_lt_i32 s10, 0x8000
	v_add_u32_e32 v38, s7, v38
	s_nop 0
	ds_read_b128 v[48:51], v72 offset:38912
	v_mfma_f32_16x16x32_f16 v[18:21], v[30:33], v[56:59], v[18:21]
	ds_read_b128 v[30:33], v72 offset:39936
	s_nop 1
	v_cvt_pk_f16_f32 v1, v28, v29
	v_cvt_pk_f16_f32 v0, v26, v27
	s_waitcnt lgkmcnt(1)
	v_mfma_f32_16x16x32_f16 v[34:37], v[48:51], v[34:37], v[60:63]
	v_pk_max_f16 v27, v1, 0
	v_cvt_pk_f16_f32 v1, v20, v21
	v_pk_max_f16 v26, v0, 0
	v_mfma_f32_16x16x32_f16 v[20:23], v[48:51], v[22:25], v[60:63]
	v_cvt_pk_f16_f32 v0, v18, v19
	v_pk_max_f16 v18, v0, 0
	v_pk_max_f16 v19, v1, 0
	s_waitcnt lgkmcnt(0)
	v_mfma_f32_16x16x32_f16 v[34:37], v[30:33], v[52:55], v[34:37]
	v_mfma_f32_16x16x32_f16 v[20:23], v[30:33], v[56:59], v[20:23]
	s_nop 6
	v_cvt_pk_f16_f32 v0, v34, v35
	v_cvt_pk_f16_f32 v1, v36, v37
	v_pk_max_f16 v28, v0, 0
	v_pk_max_f16 v29, v1, 0
	v_cvt_pk_f16_f32 v0, v20, v21
	v_cvt_pk_f16_f32 v1, v22, v23
	v_pk_max_f16 v20, v0, 0
	v_pk_max_f16 v21, v1, 0
	v_mfma_f32_16x16x32_f16 v[24:27], v[44:47], v[26:29], 0
	s_nop 0
	v_mfma_f32_16x16x32_f16 v[18:21], v[44:47], v[18:21], 0
	s_nop 7
	v_cndmask_b32_e64 v18, v24, v18, s[0:1]
	s_cbranch_scc0 .LBB0_37
.LBB0_35:
	s_setprio 3
	s_cmp_lt_u32 s33, 6
	s_cbranch_scc1 .Lprio_done
	s_setprio 2
	s_cmp_lt_u32 s33, 7
	s_cbranch_scc1 .Lprio_done
	s_setprio 1
	s_cmp_lt_u32 s33, 8
	s_cbranch_scc1 .Lprio_done
	s_setprio 0
